# attn: key-tile rotation (2qb+25head)&31
# speedup vs baseline: 1.0036x; 1.0036x over previous
.Lp_top:
	s_lshl_b32 s6, s21, 20
	s_add_u32 s4, s4, s6
	s_addc_u32 s5, s5, 0
	v_lshlrev_b32_e32 v54, 4, v0
	v_mov_b32_e32 v55, v63
	s_lshl_b32 s3, s3, 1
	s_mul_i32 s20, s21, 25
	v_lshl_add_u64 v[4:5], s[4:5], 0, v[54:55]
	s_mov_b64 s[4:5], 0x1000000
	s_add_i32 s20, s20, s3
	v_lshl_add_u64 v[170:171], v[4:5], 0, s[4:5]
	s_and_b32 s22, s20, 31
	s_lshl_b32 s4, s20, 12
	s_lshl_b32 s12, s22, 13
	s_add_i32 s5, s4, 0x1000
	v_lshl_add_u64 v[58:59], v[170:171], 0, s[12:13]
	s_mov_b32 s3, 0x80000
	s_and_b32 s5, s5, 0x1f000
	v_add_co_u32_e32 v16, vcc, s3, v58
	s_lshl_b32 s12, s5, 1
	s_nop 0
	v_addc_co_u32_e32 v17, vcc, 0, v59, vcc
	v_lshl_add_u64 v[56:57], v[170:171], 0, s[12:13]
	global_load_dwordx4 v[4:7], v[58:59], off
	global_load_dwordx4 v[8:11], v[56:57], off
	global_load_dwordx4 v[12:15], v[16:17], off
	v_add_co_u32_e32 v16, vcc, s3, v56
	v_lshrrev_b32_e32 v184, 8, v0
	s_nop 0
	v_addc_co_u32_e32 v17, vcc, 0, v57, vcc
	global_load_dwordx4 v[16:19], v[16:17], off
	v_and_b32_e32 v20, 19, v0
	v_lshlrev_b32_e32 v21, 1, v0
	v_and_b32_e32 v2, 4, v2
	v_and_or_b32 v20, v21, 8, v20
	v_lshlrev_b32_e32 v101, 5, v184
	s_addk_i32 s4, 0x2000
	v_or3_b32 v2, v20, v2, v101
	s_and_b32 s4, s4, 0x1f000
	v_mul_u32_u24_e32 v2, 0x48, v2
	s_lshl_b32 s12, s4, 1
	v_lshlrev_b32_e32 v3, 3, v0
	v_lshlrev_b32_e32 v100, 1, v99
	v_lshlrev_b32_e32 v2, 1, v2
	v_lshl_add_u64 v[60:61], v[170:171], 0, s[12:13]
	v_and_b32_e32 v3, 56, v3
	v_add3_u32 v186, 0, v2, v100
	v_add_co_u32_e32 v2, vcc, s3, v60
	v_lshlrev_b32_e32 v68, 1, v3
	s_nop 0
	v_addc_co_u32_e32 v3, vcc, 0, v61, vcc
	global_load_dwordx4 v[162:165], v[60:61], off
	global_load_dwordx4 v[166:169], v[2:3], off
	v_lshrrev_b32_e32 v82, 3, v0
	v_mul_u32_u24_e32 v22, 0x48, v82
	v_lshlrev_b32_e32 v21, 1, v22
	v_add3_u32 v185, 0, v21, v68
	s_mov_b64 s[24:25], 0x80000
	s_add_i32 s17, s20, 3
	s_add_i32 s18, s20, 4
	v_mov_b32_e32 v62, v63
	v_lshrrev_b32_e32 v55, 6, v0
	v_mov_b32_e32 v83, 0
	v_mov_b32_e32 v84, 0
	v_lshl_add_u64 v[70:71], v[58:59], 0, s[24:25]
	v_lshl_add_u64 v[66:67], v[56:57], 0, s[24:25]
	v_lshl_add_u64 v[64:65], v[60:61], 0, s[24:25]
	s_waitcnt vmcnt(5)
	ds_write_b128 v185, v[4:7]
	s_waitcnt vmcnt(3)
	ds_write_b128 v185, v[12:15] offset:9216
	ds_write_b128 v185, v[8:11] offset:18432
	s_waitcnt vmcnt(2)
	ds_write_b128 v185, v[16:19] offset:27648
	s_waitcnt lgkmcnt(0)
	s_barrier
	ds_read_b128 v[2:5], v186
	ds_read_b128 v[38:41], v186 offset:32
	s_waitcnt lgkmcnt(1)
	v_mfma_f32_32x32x16_f16 v[2:17], v[2:5], v[114:117], 0
	ds_read_b128 v[18:21], v186 offset:9216
	ds_read_b128 v[46:49], v186 offset:9248
	s_waitcnt lgkmcnt(1)
	v_mfma_f32_32x32x16_f16 v[18:33], v[18:21], v[130:133], 0
	v_mfma_f32_32x32x16_f16 v[2:17], v[38:41], v[118:121], v[2:17]
	s_waitcnt lgkmcnt(0)
	v_mfma_f32_32x32x16_f16 v[18:33], v[46:49], v[134:137], v[18:33]
	ds_read_b128 v[38:41], v186 offset:64
	ds_read_b128 v[46:49], v186 offset:96
	s_waitcnt lgkmcnt(1)
	v_mfma_f32_32x32x16_f16 v[2:17], v[38:41], v[122:125], v[2:17]
	ds_read_b128 v[38:41], v186 offset:9280
	ds_read_b128 v[50:53], v186 offset:9312
	s_load_dwordx4 s[4:7], s[0:1], 0x38
	s_load_dwordx2 s[14:15], s[0:1], 0x8
	s_mov_b32 s0, -2
	s_mov_b32 s1, 0x3f800000
	s_waitcnt lgkmcnt(0)
	s_barrier
	v_mfma_f32_32x32x16_f16 v[18:33], v[38:41], v[138:141], v[18:33]
	v_mfma_f32_32x32x16_f16 v[2:17], v[46:49], v[126:129], v[2:17]
	v_mfma_f32_32x32x16_f16 v[18:33], v[50:53], v[142:145], v[18:33]
	s_lshl_b32 s12, s17, 13
	s_and_b32 s12, s12, 0x3e000
	s_add_u32 s28, s12, s3
	s_mov_b32 s29, 0
	v_lshl_add_u64 v[176:177], v[170:171], 0, s[12:13]
	global_load_dwordx4 v[50:53], v[176:177], off
	v_lshl_add_u64 v[176:177], v[170:171], 0, s[28:29]
	global_load_dwordx4 v[94:97], v[176:177], off
	s_nop 7
	s_cmp_eq_u32 s37, 1
	s_cbranch_scc0 .Lf_A
	v_mov_b32_e32 v83, 0xf149f2ca
	v_mov_b32_e32 v84, 0xf149f2ca
	s_branch .Ls_A

.Ll1_cont:
	ds_bpermute_b32 v2, v69, v84
	ds_bpermute_b32 v5, v69, v83
	v_max_f32_e32 v4, v84, v84
	v_max_f32_e32 v7, v83, v83
	ds_bpermute_b32 v3, v69, v63
	s_waitcnt lgkmcnt(2)
	v_max_f32_e32 v6, v2, v2
	v_max_f32_e32 v4, v4, v6
	v_sub_f32_e32 v6, v84, v4
	v_exp_f32_e32 v9, v6
	s_waitcnt lgkmcnt(1)
	v_max_f32_e32 v6, v5, v5
	v_sub_f32_e32 v2, v2, v4
	v_max_f32_e32 v6, v7, v6
	v_exp_f32_e32 v11, v2
	ds_bpermute_b32 v2, v69, v62
	v_sub_f32_e32 v5, v5, v6
	v_sub_f32_e32 v7, v83, v6
	v_exp_f32_e32 v10, v5
	v_exp_f32_e32 v8, v7
	v_cmp_gt_u32_e32 vcc, 32, v98
	s_waitcnt lgkmcnt(0)
	v_pk_mul_f32 v[2:3], v[10:11], v[2:3]
	s_nop 0
	v_pk_fma_f32 v[8:9], v[62:63], v[8:9], v[2:3]
	v_lshlrev_b32_e32 v2, 7, v184
	v_or3_b32 v10, v183, v2, v1
	s_and_saveexec_b64 s[0:1], vcc
	v_lshl_add_u32 v2, v10, 4, 0
	v_add_u32_e32 v2, 0x21000, v2
	v_mov_b32_e32 v5, v9
	v_mov_b32_e32 v7, v8
	ds_write_b128 v2, v[4:7]
	s_or_b64 exec, exec, s[0:1]
	s_lshl_b32 s12, s21, 7
	s_mov_b32 s3, 0
	v_or_b32_e32 v2, s12, v82
	s_lshl_b32 s13, s21, 11
	s_add_i32 s23, 0, 0x12000
	v_lshlrev_b32_e32 v2, 12, v2
	v_mov_b32_e32 v3, 0
	s_add_i32 s13, s13, s16
	s_lshl_b64 s[0:1], s[2:3], 13
	v_lshl_add_u64 v[12:13], s[14:15], 0, v[2:3]
	v_mov_b32_e32 v69, v3
	s_add_u32 s0, s10, s0
	v_lshl_add_u64 v[172:173], v[12:13], 0, v[68:69]
	s_addc_u32 s1, s11, s1
	s_lshl_b32 s10, s22, 7
	s_mov_b32 s11, s3
	s_waitcnt vmcnt(1)
	v_lshl_add_u64 v[36:37], v[172:173], 0, s[10:11]
	s_mov_b32 s10, 0x40000
	v_add_co_u32_e32 v38, vcc, s10, v36
	s_waitcnt lgkmcnt(0)
	s_barrier
	global_load_dwordx4 v[12:15], v[58:59], off
	global_load_dwordx4 v[16:19], v[70:71], off
	v_addc_co_u32_e32 v39, vcc, 0, v37, vcc
	global_load_dwordx4 v[20:23], v[56:57], off
	global_load_dwordx4 v[24:27], v[66:67], off
	global_load_dwordx4 v[28:31], v[36:37], off
	global_load_dwordx4 v[32:35], v[38:39], off
	v_add_f32_e32 v2, v78, v80
	s_movk_i32 s11, 0x1200
	v_add_f32_e32 v5, v79, v81
	s_mov_b32 s14, 0x3fb8aa3b
	v_lshlrev_b32_e32 v10, 4, v10
	v_mov_b32_e32 v36, s23
	v_mul_f32_e32 v37, 0x3fb8aa3b, v2
	v_mul_f32_e32 v38, 0x3fb8aa3b, v5
	v_xor_b32_e32 v10, 0x800, v10
	v_mad_u32_u24 v40, v55, s11, v36
	v_fma_f32 v36, v2, s14, -v37
	v_rndne_f32_e32 v39, v37
	v_fma_f32 v41, v5, s14, -v38
	s_waitcnt vmcnt(6)
	v_rndne_f32_e32 v42, v38
	v_add_u32_e32 v10, 0, v10
	v_fmac_f32_e32 v36, 0x32a5705f, v2
	v_sub_f32_e32 v37, v37, v39
	v_fmac_f32_e32 v41, 0x32a5705f, v5
	v_sub_f32_e32 v38, v38, v42
	v_add_u32_e32 v10, 0x21000, v10
	v_add_f32_e32 v44, v37, v36
	global_load_dwordx4 v[146:149], v[60:61], off
	global_load_dwordx4 v[150:153], v[64:65], off
	v_cvt_i32_f32_e32 v43, v39
	v_add_f32_e32 v41, v38, v41
	ds_read_b128 v[36:39], v10
	v_exp_f32_e32 v10, v44
	v_cvt_i32_f32_e32 v42, v42
	v_exp_f32_e32 v41, v41
	s_mov_b32 s21, 0xc2ce8ed0
	s_lshl_b32 s11, s20, 6
	s_add_i32 s14, s11, 64
	v_ldexp_f32 v10, v10, v43
	v_cmp_ngt_f32_e32 vcc, s21, v2
	s_mov_b32 s22, 0x42b17218
	s_and_b32 s14, s14, 0x7c0
	v_ldexp_f32 v41, v41, v42
	v_cndmask_b32_e32 v10, 0, v10, vcc
	v_cmp_ngt_f32_e32 vcc, s21, v5
	v_mov_b32_e32 v7, 0x7f800000
	v_max_f32_e32 v11, v4, v4
	s_mov_b32 s15, s3
	s_lshl_b32 s14, s14, 1
	s_waitcnt lgkmcnt(0)
	v_max_f32_e32 v42, v36, v36
	v_cndmask_b32_e32 v41, 0, v41, vcc
	v_cmp_nlt_f32_e32 vcc, s22, v2
	v_max_f32_e32 v187, v11, v42
	v_mov_b32_e32 v55, v3
	v_cndmask_b32_e32 v2, v7, v10, vcc
	v_cmp_nlt_f32_e32 vcc, s22, v5
	v_lshl_add_u64 v[10:11], v[172:173], 0, s[14:15]
	v_lshl_add_u64 v[178:179], s[0:1], 0, v[54:55]
	v_cndmask_b32_e32 v5, v7, v41, vcc
	v_sub_f32_e32 v2, v2, v5
	v_add_f32_e32 v41, 0x3e4ccccd, v2
	v_sub_f32_e32 v2, v4, v187
	v_max_f32_e32 v4, v6, v6
	s_and_b32 s1, s2, 7
	s_mulk_i32 s1, 0xc80
	s_mulk_i32 s19, 0x640
	s_add_i32 s0, s20, 2
	s_waitcnt vmcnt(7)
	ds_write_b128 v185, v[12:15]
	s_waitcnt vmcnt(6)
	ds_write_b128 v185, v[16:19] offset:9216
	s_waitcnt vmcnt(5)
	ds_write_b128 v185, v[20:23] offset:18432
	s_waitcnt vmcnt(4)
	ds_write_b128 v185, v[24:27] offset:27648
	s_waitcnt vmcnt(3)
	ds_write_b128 v185, v[28:31] offset:36864
	s_waitcnt vmcnt(2)
	ds_write_b128 v185, v[32:35] offset:46080
	v_add_co_u32_e32 v12, vcc, s10, v10
	v_exp_f32_e32 v23, v2
	s_nop 0
	v_addc_co_u32_e32 v13, vcc, 0, v11, vcc
	global_load_dwordx4 v[154:157], v[10:11], off
	global_load_dwordx4 v[158:161], v[12:13], off
	s_waitcnt lgkmcnt(0)
	s_barrier
	ds_read_b128 v[10:13], v186
	v_sub_f32_e32 v2, v36, v187
	v_exp_f32_e32 v25, v2
	v_max_f32_e32 v2, v38, v38
	v_max_f32_e32 v188, v4, v2
	v_sub_f32_e32 v2, v6, v188
	v_exp_f32_e32 v22, v2
	v_sub_f32_e32 v2, v38, v188
	v_exp_f32_e32 v24, v2
	ds_read_b128 v[14:17], v186 offset:9216
	ds_read_b128 v[18:21], v186 offset:32
	s_waitcnt lgkmcnt(2)
	v_mfma_f32_32x32x16_f16 v[66:81], v[10:13], v[114:117], 0
	v_mov_b32_e32 v36, v39
	v_mul_f32_e64 v10, v36, v24
	v_mul_f32_e64 v11, v37, v25
	ds_read_b128 v[4:7], v186 offset:9248
	s_add_i32 s1, s1, s19
	s_mov_b32 s14, 0x30000
	s_mov_b32 s15, 0x80000
	s_mov_b32 s19, 0
	s_waitcnt lgkmcnt(2)
	v_mfma_f32_32x32x16_f16 v[82:97], v[14:17], v[130:133], 0
	v_fma_f32 v16, v8, v22, v10
	v_fma_f32 v17, v9, v23, v11
	v_log_f32_e32 v238, v17
	s_nop 0
	v_add_f32_e32 v187, v187, v238
	v_sub_f32_e32 v240, 0, v187
	v_sub_f32_e32 v241, 0, v187
	v_sub_f32_e32 v242, 0, v187
	v_sub_f32_e32 v243, 0, v187
	v_sub_f32_e32 v244, 0, v187
	v_sub_f32_e32 v245, 0, v187
	v_sub_f32_e32 v246, 0, v187
	v_sub_f32_e32 v247, 0, v187
	v_sub_f32_e32 v248, 0, v187
	v_sub_f32_e32 v249, 0, v187
	v_sub_f32_e32 v250, 0, v187
	v_sub_f32_e32 v251, 0, v187
	v_sub_f32_e32 v252, 0, v187
	v_sub_f32_e32 v253, 0, v187
	v_sub_f32_e32 v254, 0, v187
	v_sub_f32_e32 v255, 0, v187
	v_lshrrev_b32_e32 v22, 3, v98
	v_or3_b32 v2, s13, v183, v22
	v_lshlrev_b64 v[8:9], 13, v[2:3]
	v_lshl_add_u64 v[8:9], s[4:5], 0, v[8:9]
	v_lshlrev_b32_e32 v2, 2, v101
	v_lshl_add_u64 v[8:9], v[8:9], 0, v[2:3]
	v_and_b32_e32 v2, 0x70, v54
	v_lshl_add_u64 v[174:175], v[8:9], 0, v[2:3]
	ds_read_b128 v[8:11], v186 offset:64
	s_waitcnt lgkmcnt(2)
	v_mfma_f32_32x32x16_f16 v[66:81], v[18:21], v[118:121], v[66:81]
	v_div_scale_f32 v18, s[4:5], v16, v16, -v41
	v_rcp_f32_e32 v19, v18
	v_div_scale_f32 v20, vcc, -v41, v16, -v41
	s_mov_b32 s13, 0x20000
	v_mov_b32_e32 v24, v3
	s_waitcnt lgkmcnt(1)
	v_mfma_f32_32x32x16_f16 v[82:97], v[4:7], v[134:137], v[82:97]
	v_fma_f32 v4, -v18, v19, 1.0
	v_fmac_f32_e32 v19, v4, v19
	v_mul_f32_e32 v21, v20, v19
	ds_read_b128 v[4:7], v186 offset:9280
	ds_read_b128 v[12:15], v186 offset:96
	v_mov_b32_e32 v25, v3
	v_mov_b32_e32 v26, v3
	v_mov_b32_e32 v27, v3
	s_waitcnt lgkmcnt(2)
	v_mfma_f32_32x32x16_f16 v[66:81], v[8:11], v[122:125], v[66:81]
	v_fma_f32 v8, -v18, v21, v20
	v_fmac_f32_e32 v21, v8, v19
	v_fma_f32 v18, -v18, v21, v20
	v_div_scale_f32 v20, s[4:5], v17, v17, 1.0
	v_rcp_f32_e32 v23, v20
	ds_read_b128 v[8:11], v186 offset:9312
	s_waitcnt lgkmcnt(2)
	v_mfma_f32_32x32x16_f16 v[82:97], v[4:7], v[138:141], v[82:97]
	v_div_fmas_f32 v4, v18, v19, v21
	v_div_fixup_f32 v176, v4, v16, -v41
	v_fma_f32 v4, -v20, v23, 1.0
	v_fmac_f32_e32 v23, v4, v23
	v_div_scale_f32 v4, vcc, 1.0, v17, 1.0
	v_mul_f32_e32 v5, v4, v23
	v_fma_f32 v6, -v20, v5, v4
	v_fmac_f32_e32 v5, v6, v23
	s_waitcnt lgkmcnt(1)
	v_mfma_f32_32x32x16_f16 v[66:81], v[12:15], v[126:129], v[66:81]
	v_fma_f32 v4, -v20, v5, v4
	v_div_fmas_f32 v4, v4, v23, v5
	v_div_fixup_f32 v177, v4, v17, 1.0
	v_mul_u32_u24_e32 v4, 0x90, v22
	v_add3_u32 v189, v40, v4, v2
	v_mul_u32_u24_e32 v2, 0x90, v1
	v_lshlrev_b32_e32 v4, 2, v99
	s_waitcnt lgkmcnt(0)
	v_mfma_f32_32x32x16_f16 v[82:97], v[8:11], v[142:145], v[82:97]
	v_add3_u32 v190, v40, v2, v4
	v_mul_u32_u24_e32 v2, 0x48, v1
	v_lshl_add_u32 v2, v2, 1, 0
	v_lshlrev_b32_e32 v4, 1, v101
	v_add3_u32 v191, v2, v4, v100
	s_mov_b32 s4, 0x3f800000
	s_mov_b32 s5, 0x10000
	v_mov_b32_e32 v2, v3
	v_mov_b32_e32 v4, v3
	v_mov_b32_e32 v5, v3
	v_mov_b32_e32 v6, v3
	v_mov_b32_e32 v7, v3
	v_mov_b32_e32 v8, v3
	v_mov_b32_e32 v9, v3
	v_mov_b32_e32 v10, v3
	v_mov_b32_e32 v11, v3
	v_mov_b32_e32 v12, v3
	v_mov_b32_e32 v13, v3
	v_mov_b32_e32 v14, v3
	v_mov_b32_e32 v15, v3
	v_mov_b32_e32 v16, v3
	v_mov_b32_e32 v17, v3
	v_mov_b32_e32 v18, v3
	v_mov_b32_e32 v19, v3
	v_mov_b32_e32 v20, v3
	v_mov_b32_e32 v21, v3
	v_mov_b32_e32 v22, v3
	v_mov_b32_e32 v23, v3
	v_mov_b32_e32 v28, v3
	v_mov_b32_e32 v29, v3
	v_mov_b32_e32 v30, v3
	v_mov_b32_e32 v31, v3
	v_mov_b32_e32 v32, v3
	v_mov_b32_e32 v33, v3
	v_mov_b32_e32 v34, v3
	v_mov_b32_e32 v35, v3
	v_mov_b32_e32 v36, v3
	v_mov_b32_e32 v37, v3
	v_mov_b32_e32 v38, v3
	v_mov_b32_e32 v39, v3
	v_mov_b32_e32 v40, v3
	v_mov_b32_e32 v41, v3
	v_mov_b32_e32 v42, v3
	v_mov_b32_e32 v43, v3
	v_mov_b32_e32 v44, v3
	v_mov_b32_e32 v45, v3
	v_mov_b32_e32 v46, v3
	v_mov_b32_e32 v47, v3
	v_mov_b32_e32 v48, v3
	v_mov_b32_e32 v49, v3
	v_mov_b32_e32 v50, v3
	v_mov_b32_e32 v51, v3
	v_mov_b32_e32 v52, v3
	v_mov_b32_e32 v53, v3
	v_mov_b32_e32 v54, v3
	v_mov_b32_e32 v56, v3
	v_mov_b32_e32 v57, v3
	v_mov_b32_e32 v58, v3
	v_mov_b32_e32 v59, v3
	v_mov_b32_e32 v60, v3
	v_mov_b32_e32 v61, v3
	v_mov_b32_e32 v62, v3
	v_mov_b32_e32 v63, v3
	v_mov_b32_e32 v64, v3
	v_mov_b32_e32 v65, v3
	v_add_u32_e32 v192, 0xd800, v191
	v_sub_f32_e32 v66, v66, v187
	v_sub_f32_e32 v67, v67, v187
	v_sub_f32_e32 v68, v68, v187
	v_sub_f32_e32 v69, v69, v187
	v_sub_f32_e32 v70, v70, v187
	v_sub_f32_e32 v71, v71, v187
	v_sub_f32_e32 v72, v72, v187
	v_sub_f32_e32 v73, v73, v187
	v_sub_f32_e32 v74, v74, v187
	v_sub_f32_e32 v75, v75, v187
	v_sub_f32_e32 v76, v76, v187
	v_sub_f32_e32 v77, v77, v187
	v_sub_f32_e32 v78, v78, v187
	v_sub_f32_e32 v79, v79, v187
	v_sub_f32_e32 v80, v80, v187
	v_sub_f32_e32 v81, v81, v187
	s_mov_b32 s27, 0x42c80000
	v_cmp_gt_f32_e64 vcc, |v188|, s27
	s_cbranch_vccnz .Ll2_gen
	v_sub_f32_e32 v238, 0, v188
	v_exp_f32_e32 v238, v238
	s_nop 0
	v_mul_f32_e32 v176, v176, v238
	s_barrier
	s_branch .Ll2f_top
